# baseline (speedup 1.0000x reference)
.LBB3_36:
	s_andn2_b64 vcc, exec, s[6:7]
	s_cbranch_vccnz .LBB3_86
	s_cmpk_gt_u32 s2, 0xff
	s_cbranch_scc1 .LBB3_86
	s_mov_b64 s[40:41], s[0:1]
	s_mov_b32 s44, s18
	s_mov_b32 s45, s19
	s_mov_b32 s46, 0
	s_mov_b32 s60, s2
	s_mov_b32 s61, 0
	s_mov_b32 s65, 0
	s_mov_b32 s84, 0
	s_mov_b32 s85, 0
	s_mov_b32 s88, 0
	s_mov_b32 s73, 0
	v_readfirstlane_b32 s72, v0
	s_nop 3
	s_cmp_ge_u32 s72, 0x100
	s_cselect_b32 s79, 1, 0
	s_load_dwordx2 s[68:69], s[0:1], 0x0
	s_load_dwordx2 s[70:71], s[0:1], 0x38
	s_mov_b32 s49, 0
	s_mov_b32 s47, 0
	s_mov_b32 s48, 0
	s_movk_i32 s50, 27
	s_load_dwordx2 s[52:53], s[0:1], 0x30
	s_add_i32 s51, s19, 31
	s_lshr_b32 s51, s51, 5
	s_sub_i32 s51, s51, 0x200
	s_sub_i32 s55, s51, 1
	s_cmp_lt_u32 s55, 0x80
	s_cselect_b32 s51, s51, 0
	v_mov_b32_e32 v248, v0
.Lgru_tile:
	s_cmp_eq_u32 s47, 1
	s_cselect_b32 s67, 8, 17
	s_movk_i32 s87, 0x63
	s_cmp_lg_u32 s46, 0
	s_cbranch_scc1 .Lgru_tile_alt
	s_load_dwordx8 s[8:15], s[0:1], 0x0
	s_load_dwordx2 s[2:3], s[0:1], 0x20
	v_lshlrev_b32_e32 v52, 4, v0
	v_mov_b32_e32 v53, 0
	s_movk_i32 s6, 0x100
	s_waitcnt lgkmcnt(0)
	v_lshl_add_u64 v[30:31], s[14:15], 0, v[52:53]
	v_add_co_u32_e32 v14, vcc, 0x2000, v30
	v_bfe_u32 v55, v0, 6, 2
	s_nop 0
	v_addc_co_u32_e32 v15, vcc, 0, v31, vcc
	v_add_co_u32_e32 v22, vcc, 0x6000, v30
	v_mov_b32_e32 v46, s3
	s_nop 0
	v_addc_co_u32_e32 v23, vcc, 0, v31, vcc
	v_add_co_u32_e32 v32, vcc, 0xa000, v30
	v_mov_b32_e32 v47, s13
	s_nop 0
	v_addc_co_u32_e32 v33, vcc, 0, v31, vcc
	v_add_co_u32_e32 v38, vcc, 0xe000, v30
	v_mov_b32_e32 v48, s12
	s_nop 0
	v_addc_co_u32_e32 v39, vcc, 0, v31, vcc
	v_cmp_gt_u32_e32 vcc, s6, v0
	v_mul_u32_u24_e32 v54, 0x540, v55
	v_mov_b32_e32 v49, v53
	v_cndmask_b32_e32 v47, v46, v47, vcc
	v_mov_b32_e32 v46, s2
	v_cndmask_b32_e32 v46, v46, v48, vcc
	v_lshlrev_b32_e32 v48, 4, v54
	v_lshl_add_u64 v[46:47], v[46:47], 0, v[48:49]
	v_lshlrev_b32_e32 v50, 4, v1
	v_mov_b32_e32 v51, v53
	s_movk_i32 s5, 0x1000
	v_lshl_add_u64 v[46:47], v[46:47], 0, v[50:51]
	v_add_co_u32_e32 v48, vcc, s5, v46
	s_movk_i32 s4, 0x2000
	s_nop 0
	v_addc_co_u32_e32 v49, vcc, 0, v47, vcc
	v_or_b32_e32 v56, 0x400, v0
	v_add_co_u32_e32 v60, vcc, s4, v46
	v_lshlrev_b32_e32 v16, 4, v56
	v_or_b32_e32 v24, 0x8000, v52
	v_or_b32_e32 v34, 0xc000, v52
	v_or_b32_e32 v30, 0x1000, v0
	v_addc_co_u32_e32 v61, vcc, 0, v47, vcc
	s_movk_i32 s2, 0x3000
	global_load_dwordx4 v[2:5], v52, s[14:15]
	global_load_dwordx4 v[6:9], v[14:15], off
	global_load_dwordx4 v[10:13], v16, s[14:15]
	s_nop 0
	global_load_dwordx4 v[14:17], v[22:23], off
	global_load_dwordx4 v[18:21], v24, s[14:15]
	s_nop 0
	global_load_dwordx4 v[22:25], v[32:33], off
	global_load_dwordx4 v[26:29], v34, s[14:15]
	v_lshlrev_b32_e32 v57, 4, v30
	global_load_dwordx4 v[30:33], v[38:39], off
	global_load_dwordx4 v[34:37], v57, s[14:15]
	v_or_b32_e32 v38, 0x1200, v0
	v_add_co_u32_e32 v62, vcc, s2, v46
	v_lshlrev_b32_e32 v58, 4, v38
	v_or_b32_e32 v38, 0x1400, v0
	v_addc_co_u32_e32 v63, vcc, 0, v47, vcc
	s_movk_i32 s2, 0x4000
	v_min_u32_e32 v38, 0x14ff, v38
	v_add_co_u32_e32 v64, vcc, s2, v46
	v_lshlrev_b32_e32 v59, 4, v38
	global_load_dwordx4 v[38:41], v58, s[14:15]
	global_load_dwordx4 v[42:45], v59, s[14:15]
	global_load_dwordx4 v[82:85], v[46:47], off
	global_load_dwordx4 v[86:89], v[46:47], off offset:1024
	global_load_dwordx4 v[90:93], v[46:47], off offset:2048
	global_load_dwordx4 v[94:97], v[46:47], off offset:3072
	global_load_dwordx4 v[98:101], v[48:49], off offset:1024
	global_load_dwordx4 v[102:105], v[48:49], off offset:2048
	global_load_dwordx4 v[106:109], v[60:61], off offset:-4096
	global_load_dwordx4 v[110:113], v[60:61], off
	global_load_dwordx4 v[114:117], v[60:61], off offset:1024
	global_load_dwordx4 v[118:121], v[60:61], off offset:2048
	v_addc_co_u32_e32 v65, vcc, 0, v47, vcc
	global_load_dwordx4 v[122:125], v[60:61], off offset:3072
	global_load_dwordx4 v[126:129], v[64:65], off offset:-4096
	global_load_dwordx4 v[130:133], v[48:49], off offset:3072
	global_load_dwordx4 v[134:137], v[62:63], off offset:1024
	global_load_dwordx4 v[138:141], v[62:63], off offset:2048
	global_load_dwordx4 v[142:145], v[62:63], off offset:3072
	global_load_dwordx4 v[146:149], v[64:65], off
	global_load_dwordx4 v[150:153], v[64:65], off offset:1024
	global_load_dwordx4 v[154:157], v[64:65], off offset:2048
	global_load_dwordx4 v[158:161], v[64:65], off offset:3072
	v_add_co_u32_e32 v46, vcc, 0x5000, v46
	s_movk_i32 s2, 0xff
	s_nop 0
	v_addc_co_u32_e32 v47, vcc, 0, v47, vcc
	global_load_dwordx4 v[162:165], v[46:47], off

.Lgru_noflag:
	s_cmp_eq_u32 s84, 0
	s_cbranch_scc1 .Lpp_normal
	s_mov_b32 s84, 0
	s_cmp_eq_u32 s85, 0
	s_cbranch_scc1 .Lpp_nocopy
	v_lshlrev_b32_e32 v4, 4, v0
	v_add_u32_e32 v5, 0x400, v0
	v_min_u32_e32 v5, 0x55f, v5
	v_lshlrev_b32_e32 v5, 4, v5
	v_add_u32_e32 v6, 0x1a600, v4
	v_add_u32_e32 v7, 0x1a600, v5
	ds_read_b128 v[8:11], v6
	ds_read_b128 v[12:15], v6 offset:8192
	ds_read_b128 v[16:19], v7
	v_add_u32_e32 v6, 0x15000, v4
	v_add_u32_e32 v7, 0x15000, v5
	s_waitcnt lgkmcnt(0)
	ds_write_b128 v6, v[8:11]
	ds_write_b128 v6, v[12:15] offset:8192
	ds_write_b128 v7, v[16:19]
.Lpp_nocopy:
	v_cmp_gt_u32_e32 vcc, 2, v2
	v_lshlrev_b32_e32 v192, 3, v2
	v_bfe_u32 v0, v0, 3, 5
	v_cndmask_b32_e64 v3, 32, 40, vcc
	v_or_b32_e32 v3, v3, v2
	v_lshlrev_b32_e32 v190, 3, v3
	s_mov_b64 s[4:5], exec
	s_branch .LBB3_61

.LBB3_62:
	s_sub_i32 s66, s14, s67
	s_cmp_gt_u32 s66, 5
	s_cbranch_scc1 .Lpf_done
	s_cmp_eq_u32 s66, 0
	s_cbranch_scc1 .Lpf_0
	s_cmp_eq_u32 s73, 0
	s_cbranch_scc1 .Lpf_done
	s_cmp_eq_u32 s66, 1
	s_cbranch_scc1 .Lpf_1
	s_cmp_eq_u32 s66, 2
	s_cbranch_scc1 .Lpf_2
	s_cmp_eq_u32 s66, 5
	s_cbranch_scc1 .Lpf_5
	s_cmp_eq_u32 s66, 4
	s_cbranch_scc1 .Lpf_done
	s_waitcnt vmcnt(0)

.LBB3_71:
	s_andn2_b64 vcc, exec, s[8:9]
	s_cbranch_vccnz .LBB3_73
	s_setprio 1
	ds_read_b128 v[64:67], v213
	s_mul_i32 s8, s20, 0x5600
	v_add_u32_e32 v0, s8, v212
	s_waitcnt vmcnt(6)
	ds_read2_b64 v[2:5], v0 offset1:1
	ds_read_b128 v[220:223], v213 offset:1024
	ds_read2_b64 v[34:37], v0 offset0:4 offset1:5
	s_waitcnt vmcnt(2)
	ds_read2_b64 v[18:21], v0 offset0:28 offset1:29
	ds_read2_b64 v[38:41], v0 offset0:32 offset1:33
	s_mul_i32 s8, s20, 0x1e00
	v_add_u32_e32 v63, s8, v211
	s_min_u32 s8, s14, 22
	s_cmp_gt_u32 s14, s87
	s_cbranch_scc0 .Lpp_idx
	s_sub_i32 s8, s14, s87
	s_add_i32 s8, s8, s88
	s_sub_i32 s8, s8, 3
.Lpp_idx:
	s_waitcnt vmcnt(0) lgkmcnt(1)
	v_mfma_f32_32x32x16_f16 v[18:33], v[64:67], v[18:21], 0
	v_mfma_f32_32x32x16_f16 v[2:17], v[64:67], v[2:5], 0
	s_waitcnt lgkmcnt(0)
	v_mfma_f32_32x32x16_f16 v[18:33], v[220:223], v[38:41], v[18:33]
	v_mfma_f32_32x32x16_f16 v[2:17], v[220:223], v[34:37], v[2:17]
	ds_read_b128 v[34:37], v63
	ds_read_b128 v[68:71], v63 offset:32
	s_waitcnt lgkmcnt(1)
	v_mfma_f32_32x32x16_f16 v[18:33], v[130:133], v[34:37], v[18:33]
	v_mfma_f32_32x32x16_f16 v[2:17], v[82:85], v[34:37], v[2:17]
	v_mfma_f32_32x32x16_f16 v[34:49], v[138:141], v[34:37], 0
	s_waitcnt lgkmcnt(0)
	v_mfma_f32_32x32x16_f16 v[18:33], v[110:113], v[68:71], v[18:33]
	v_mfma_f32_32x32x16_f16 v[2:17], v[86:89], v[68:71], v[2:17]
	v_mfma_f32_32x32x16_f16 v[34:49], v[142:145], v[68:71], v[34:49]
	ds_read_b128 v[68:71], v63 offset:64
	ds_read_b128 v[72:75], v63 offset:96
	s_waitcnt lgkmcnt(1)
	v_mfma_f32_32x32x16_f16 v[18:33], v[114:117], v[68:71], v[18:33]
	v_mfma_f32_32x32x16_f16 v[2:17], v[90:93], v[68:71], v[2:17]
	v_mfma_f32_32x32x16_f16 v[34:49], v[146:149], v[68:71], v[34:49]
	s_waitcnt lgkmcnt(0)
	v_mfma_f32_32x32x16_f16 v[18:33], v[118:121], v[72:75], v[18:33]
	v_mfma_f32_32x32x16_f16 v[2:17], v[94:97], v[72:75], v[2:17]
	v_mfma_f32_32x32x16_f16 v[34:49], v[150:153], v[72:75], v[34:49]
	ds_read_b128 v[68:71], v63 offset:128
	ds_read_b128 v[72:75], v63 offset:160
	s_waitcnt lgkmcnt(1)
	v_mfma_f32_32x32x16_f16 v[18:33], v[122:125], v[68:71], v[18:33]
	s_waitcnt lgkmcnt(0)
	v_mfma_f32_32x32x16_f16 v[18:33], v[126:129], v[72:75], v[18:33]
	v_mfma_f32_32x32x16_f16 v[2:17], v[106:109], v[68:71], v[2:17]
	v_mfma_f32_32x32x16_f16 v[34:49], v[154:157], v[68:71], v[34:49]
	ds_read_b128 v[68:71], v63 offset:192
	v_lshl_add_u32 v63, s8, 2, v214
	ds_read_b32 v63, v63 offset:8
	s_mul_i32 s8, s19, 0x5600
	s_waitcnt lgkmcnt(1)
	v_mfma_f32_32x32x16_f16 v[18:33], v[134:137], v[68:71], v[18:33]
	v_mfma_f32_32x32x16_f16 v[2:17], v[98:101], v[72:75], v[2:17]
	v_mfma_f32_32x32x16_f16 v[34:49], v[158:161], v[72:75], v[34:49]
	ds_read2_b64 v[72:75], v0 offset0:56 offset1:57
	ds_read2_b64 v[224:227], v0 offset0:60 offset1:61
	s_waitcnt lgkmcnt(2)
	v_mad_u32_u24 v228, v63, s18, v240
	v_add_u32_e32 v31, s8, v242
	ds_write_b128 v31, v[178:181]
	ds_write_b128 v31, v[174:177] offset:128
	global_load_dwordx4 v[178:181], v228, s[10:11]
	global_load_dwordx4 v[174:177], v228, s[10:11] offset:128
	ds_write_b128 v31, v[170:173] offset:256
	ds_write_b128 v31, v[166:169] offset:384
	v_add_u32_e32 v0, s8, v243
	global_load_dwordx4 v[170:173], v228, s[10:11] offset:256
	global_load_dwordx4 v[166:169], v228, s[10:11] offset:384
	ds_write_b128 v31, v[186:189] offset:512
	ds_write_b128 v0, v[182:185]
	v_add_u32_e32 v229, v241, v228
	global_load_dwordx4 v[186:189], v228, s[10:11] offset:512
	global_load_dwordx4 v[182:185], v229, s[10:11]
	v_mfma_f32_32x32x16_f16 v[2:17], v[102:105], v[68:71], v[2:17]
	v_mfma_f32_32x32x16_f16 v[34:49], v[162:165], v[68:71], v[34:49]
	s_waitcnt lgkmcnt(7)
	v_mfma_f32_32x32x16_f16 v[66:81], v[64:67], v[72:75], 0
	s_waitcnt lgkmcnt(6)
	v_mfma_f32_32x32x16_f16 v[66:81], v[220:223], v[224:227], v[66:81]
	s_setprio 0

.Lpf_0:
	s_mov_b32 s88, 0
	s_mov_b32 s62, -1
	s_cmp_lg_u32 s51, 0
	s_cbranch_scc1 .Lpfs_split
	s_add_i32 s66, s44, 0x2000
	s_cmp_lt_i32 s66, s45
	s_cselect_b32 s62, s66, -1
	s_branch .Lpfs_done

.Lpfs_j2:
	s_cmp_lt_u32 s60, s51
	s_cbranch_scc1 .Lpfs_done
	s_lshl_b32 s66, s51, 1
	s_cmp_ge_u32 s60, s66
	s_cbranch_scc1 .Lpfs_none
	s_movk_i32 s88, 16
	s_sub_i32 s62, s60, s51
	s_add_i32 s62, s62, 0x200
	s_lshl_b32 s62, s62, 5
	s_branch .Lpfs_done

.Lpf_5:
	v_lshlrev_b32_e32 v219, 2, v248
	v_add_u32_e32 v219, 0x25600, v219
	v_min_u32_e32 v220, 0x11f, v248
	v_lshlrev_b32_e32 v220, 2, v220
	v_add_u32_e32 v220, 0x25e00, v220
	ds_write_b32 v219, v249
	ds_write_b32 v220, v250
	s_mov_b32 s87, s14
	s_mov_b32 s84, 1
	s_cmp_lg_u32 s47, 1
	s_cselect_b32 s85, 1, 0
	s_branch .Lpf_done
